# phase 7 (cross-attention scores): per-row 1/rms(q) pre-pass rewritten with coalesced row loads (one 1 KB row per wave instruction) and a wave-private LDS reduction; same math, f32 sum order differs
# speedup vs baseline: 1.0070x; 1.0052x over previous
; #define GAS __attribute__((address_space(1)))
; #define SB() __builtin_amdgcn_sched_barrier(0)
; __global__ void __launch_bounds__(NTHR, 2) mega_fwd(Args args) {
;     ...
;             { pg8::Unit u0; __syncthreads();
;               if (Sc.next(0, u0)) { const int r = F.tid >> 1, hf = F.tid & 1; const GAS u32x4* qp = (const GAS u32x4*)(u0.A + (size_t)r * (D * 2) + hf * 512); float ss = 0.f;
; #pragma unroll 1
;                   for (int i0 = 0; i0 < 32; i0 += 16) { u32x4 wq[16];
; #pragma unroll
;                       for (int i = 0; i < 16; ++i) wq[i] = qp[i0 + i];
;                       SB();
.LBB0_1265:
	s_cmp_le_i32 s74, s6
	s_cselect_b64 s[4:5], -1, 0
	s_cmp_lt_i32 s6, s75
	s_cselect_b64 s[6:7], -1, 0
	s_and_b64 s[44:45], s[4:5], s[6:7]
	s_andn2_b64 vcc, exec, s[44:45]
	v_mbcnt_lo_u32_b32 v0, -1, 0
	v_mbcnt_hi_u32_b32 v0, -1, v0
	s_mov_b32 s4, 0
	s_cbranch_vccnz .LBB0_1322
	s_ashr_i32 s5, s4, 31
	s_add_u32 s34, s90, s4
	s_addc_u32 s62, s91, s5
	v_readlane_b32 s4, v250, 25
	v_readlane_b32 s5, v250, 26
	s_add_u32 s6, s34, 0x2de81000
	s_addc_u32 s7, s62, 0
	s_waitcnt lgkmcnt(0)
	v_cndmask_b32_e64 v2, 0, 1, s[4:5]
	v_cmp_ne_u32_e64 s[56:57], 1, v2
	s_andn2_b64 vcc, exec, s[4:5]
	s_waitcnt vmcnt(0)
	s_barrier
	s_cbranch_vccnz .LBB0_1272
	v_readlane_b32 s4, v250, 13
	v_readlane_b32 s5, v250, 14
	v_readlane_b32 s8, v250, 15
	s_nop 3
	s_add_u32 s4, s6, s4
	s_addc_u32 s5, s7, s5
	s_add_u32 s4, s4, s8
	s_addc_u32 s5, s5, 0
	s_lshl_b32 s8, s87, 11
	s_add_u32 s36, s4, s8
	s_addc_u32 s37, s5, 0
	v_lshlrev_b32_e32 v2, 4, v0
	global_load_dwordx4 v[96:99], v2, s[36:37]
	s_add_u32 s36, s36, 0x1000
	s_addc_u32 s37, s37, 0
	global_load_dwordx4 v[100:103], v2, s[36:37]
	s_add_u32 s36, s36, 0x1000
	s_addc_u32 s37, s37, 0
	global_load_dwordx4 v[104:107], v2, s[36:37]
	s_add_u32 s36, s36, 0x1000
	s_addc_u32 s37, s37, 0
	global_load_dwordx4 v[108:111], v2, s[36:37]
	s_add_u32 s36, s36, 0x1000
	s_addc_u32 s37, s37, 0
	global_load_dwordx4 v[112:115], v2, s[36:37]
	s_add_u32 s36, s36, 0x1000
	s_addc_u32 s37, s37, 0
	global_load_dwordx4 v[116:119], v2, s[36:37]
	s_add_u32 s36, s36, 0x1000
	s_addc_u32 s37, s37, 0
	global_load_dwordx4 v[120:123], v2, s[36:37]
	s_add_u32 s36, s36, 0x1000
	s_addc_u32 s37, s37, 0
	global_load_dwordx4 v[124:127], v2, s[36:37]
	s_add_u32 s36, s36, 0x1000
	s_addc_u32 s37, s37, 0
	global_load_dwordx4 v[128:131], v2, s[36:37]
	s_add_u32 s36, s36, 0x1000
	s_addc_u32 s37, s37, 0
	global_load_dwordx4 v[132:135], v2, s[36:37]
	s_add_u32 s36, s36, 0x1000
	s_addc_u32 s37, s37, 0
	global_load_dwordx4 v[136:139], v2, s[36:37]
	s_add_u32 s36, s36, 0x1000
	s_addc_u32 s37, s37, 0
	global_load_dwordx4 v[140:143], v2, s[36:37]
	s_add_u32 s36, s36, 0x1000
	s_addc_u32 s37, s37, 0
	global_load_dwordx4 v[144:147], v2, s[36:37]
	s_add_u32 s36, s36, 0x1000
	s_addc_u32 s37, s37, 0
	global_load_dwordx4 v[148:151], v2, s[36:37]
	s_add_u32 s36, s36, 0x1000
	s_addc_u32 s37, s37, 0
	global_load_dwordx4 v[152:155], v2, s[36:37]
	s_add_u32 s36, s36, 0x1000
	s_addc_u32 s37, s37, 0
	global_load_dwordx4 v[156:159], v2, s[36:37]
	s_add_u32 s36, s36, 0x1000
	s_addc_u32 s37, s37, 0
	global_load_dwordx4 v[160:163], v2, s[36:37]
	s_add_u32 s36, s36, 0x1000
	s_addc_u32 s37, s37, 0
	global_load_dwordx4 v[164:167], v2, s[36:37]
	s_add_u32 s36, s36, 0x1000
	s_addc_u32 s37, s37, 0
	global_load_dwordx4 v[168:171], v2, s[36:37]
	s_add_u32 s36, s36, 0x1000
	s_addc_u32 s37, s37, 0
	global_load_dwordx4 v[172:175], v2, s[36:37]
	s_add_u32 s36, s36, 0x1000
	s_addc_u32 s37, s37, 0
	global_load_dwordx4 v[176:179], v2, s[36:37]
	s_add_u32 s36, s36, 0x1000
	s_addc_u32 s37, s37, 0
	global_load_dwordx4 v[180:183], v2, s[36:37]
	s_add_u32 s36, s36, 0x1000
	s_addc_u32 s37, s37, 0
	global_load_dwordx4 v[184:187], v2, s[36:37]
	s_add_u32 s36, s36, 0x1000
	s_addc_u32 s37, s37, 0
	global_load_dwordx4 v[188:191], v2, s[36:37]
	s_add_u32 s36, s36, 0x1000
	s_addc_u32 s37, s37, 0
	global_load_dwordx4 v[192:195], v2, s[36:37]
	s_add_u32 s36, s36, 0x1000
	s_addc_u32 s37, s37, 0
	global_load_dwordx4 v[196:199], v2, s[36:37]
	s_add_u32 s36, s36, 0x1000
	s_addc_u32 s37, s37, 0
	global_load_dwordx4 v[200:203], v2, s[36:37]
	s_add_u32 s36, s36, 0x1000
	s_addc_u32 s37, s37, 0
	global_load_dwordx4 v[204:207], v2, s[36:37]
	s_add_u32 s36, s36, 0x1000
	s_addc_u32 s37, s37, 0
	global_load_dwordx4 v[208:211], v2, s[36:37]
	s_add_u32 s36, s36, 0x1000
	s_addc_u32 s37, s37, 0
	global_load_dwordx4 v[212:215], v2, s[36:37]
	s_add_u32 s36, s36, 0x1000
	s_addc_u32 s37, s37, 0
	global_load_dwordx4 v[20:23], v2, s[36:37]
	s_add_u32 s36, s36, 0x1000
	s_addc_u32 s37, s37, 0
	global_load_dwordx4 v[24:27], v2, s[36:37]
	s_lshl_b32 s8, s87, 8
	v_lshl_add_u32 v3, v0, 2, s8
	v_and_b32_e32 v5, 31, v0
	v_mul_u32_u24_e32 v5, 0x110, v5
	v_lshrrev_b32_e32 v6, 5, v0
	v_lshl_add_u32 v5, v6, 7, v5
	v_add_u32_e32 v5, s8, v5
	s_waitcnt vmcnt(24)
; __device__ __forceinline__ float bflo(unsigned w) { return __uint_as_float(w << 16); }
; __device__ __forceinline__ float bfhi(unsigned w) { return __uint_as_float(w & 0xffff0000u); }
; __global__ void __launch_bounds__(NTHR, 2) mega_fwd(Args args) {
;     ...
; #pragma unroll
;                       for (int i = 0; i < 16; ++i) { const u32x4 w = wq[i]; ss += (bflo(w.x) * bflo(w.x) + bfhi(w.x) * bfhi(w.x)) + (bflo(w.y) * bflo(w.y) + bfhi(w.y) * bfhi(w.y)) + (bflo(w.z) * bflo(w.z) + bfhi(w.z) * bfhi(w.z)) + (bflo(w.w) * bflo(w.w) + bfhi(w.w) * bfhi(w.w)); } }
	v_lshlrev_b32_e32 v8, 16, v96
	v_and_b32_e32 v9, 0xffff0000, v96
	v_mul_f32_e32 v7, v8, v8
	v_fmac_f32_e32 v7, v9, v9
	v_lshlrev_b32_e32 v8, 16, v97
	v_and_b32_e32 v9, 0xffff0000, v97
	v_fmac_f32_e32 v7, v8, v8
	v_fmac_f32_e32 v7, v9, v9
	v_lshlrev_b32_e32 v8, 16, v98
	v_and_b32_e32 v9, 0xffff0000, v98
	v_fmac_f32_e32 v7, v8, v8
	v_fmac_f32_e32 v7, v9, v9
	v_lshlrev_b32_e32 v8, 16, v99
	v_and_b32_e32 v9, 0xffff0000, v99
	v_fmac_f32_e32 v7, v8, v8
	v_fmac_f32_e32 v7, v9, v9
	ds_write_b32 v3, v7
	v_lshlrev_b32_e32 v12, 16, v100
	v_and_b32_e32 v13, 0xffff0000, v100
	v_mul_f32_e32 v11, v12, v12
	v_fmac_f32_e32 v11, v13, v13
	v_lshlrev_b32_e32 v12, 16, v101
	v_and_b32_e32 v13, 0xffff0000, v101
	v_fmac_f32_e32 v11, v12, v12
	v_fmac_f32_e32 v11, v13, v13
	v_lshlrev_b32_e32 v12, 16, v102
	v_and_b32_e32 v13, 0xffff0000, v102
	v_fmac_f32_e32 v11, v12, v12
	v_fmac_f32_e32 v11, v13, v13
	v_lshlrev_b32_e32 v12, 16, v103
	v_and_b32_e32 v13, 0xffff0000, v103
	v_fmac_f32_e32 v11, v12, v12
	v_fmac_f32_e32 v11, v13, v13
	ds_write_b32 v3, v11 offset:272
	v_lshlrev_b32_e32 v8, 16, v104
	v_and_b32_e32 v9, 0xffff0000, v104
	v_mul_f32_e32 v7, v8, v8
	v_fmac_f32_e32 v7, v9, v9
	v_lshlrev_b32_e32 v8, 16, v105
	v_and_b32_e32 v9, 0xffff0000, v105
	v_fmac_f32_e32 v7, v8, v8
	v_fmac_f32_e32 v7, v9, v9
	v_lshlrev_b32_e32 v8, 16, v106
	v_and_b32_e32 v9, 0xffff0000, v106
	v_fmac_f32_e32 v7, v8, v8
	v_fmac_f32_e32 v7, v9, v9
	v_lshlrev_b32_e32 v8, 16, v107
	v_and_b32_e32 v9, 0xffff0000, v107
	v_fmac_f32_e32 v7, v8, v8
	v_fmac_f32_e32 v7, v9, v9
	ds_write_b32 v3, v7 offset:544
	v_lshlrev_b32_e32 v12, 16, v108
	v_and_b32_e32 v13, 0xffff0000, v108
	v_mul_f32_e32 v11, v12, v12
	v_fmac_f32_e32 v11, v13, v13
	v_lshlrev_b32_e32 v12, 16, v109
	v_and_b32_e32 v13, 0xffff0000, v109
	v_fmac_f32_e32 v11, v12, v12
	v_fmac_f32_e32 v11, v13, v13
	v_lshlrev_b32_e32 v12, 16, v110
	v_and_b32_e32 v13, 0xffff0000, v110
	v_fmac_f32_e32 v11, v12, v12
	v_fmac_f32_e32 v11, v13, v13
	v_lshlrev_b32_e32 v12, 16, v111
	v_and_b32_e32 v13, 0xffff0000, v111
	v_fmac_f32_e32 v11, v12, v12
	v_fmac_f32_e32 v11, v13, v13
	ds_write_b32 v3, v11 offset:816
	v_lshlrev_b32_e32 v8, 16, v112
	v_and_b32_e32 v9, 0xffff0000, v112
	v_mul_f32_e32 v7, v8, v8
	v_fmac_f32_e32 v7, v9, v9
	v_lshlrev_b32_e32 v8, 16, v113
	v_and_b32_e32 v9, 0xffff0000, v113
	v_fmac_f32_e32 v7, v8, v8
	v_fmac_f32_e32 v7, v9, v9
	v_lshlrev_b32_e32 v8, 16, v114
	v_and_b32_e32 v9, 0xffff0000, v114
	v_fmac_f32_e32 v7, v8, v8
	v_fmac_f32_e32 v7, v9, v9
	v_lshlrev_b32_e32 v8, 16, v115
	v_and_b32_e32 v9, 0xffff0000, v115
	v_fmac_f32_e32 v7, v8, v8
	v_fmac_f32_e32 v7, v9, v9
	ds_write_b32 v3, v7 offset:1088
	v_lshlrev_b32_e32 v12, 16, v116
	v_and_b32_e32 v13, 0xffff0000, v116
	v_mul_f32_e32 v11, v12, v12
	v_fmac_f32_e32 v11, v13, v13
	v_lshlrev_b32_e32 v12, 16, v117
	v_and_b32_e32 v13, 0xffff0000, v117
	v_fmac_f32_e32 v11, v12, v12
	v_fmac_f32_e32 v11, v13, v13
	v_lshlrev_b32_e32 v12, 16, v118
	v_and_b32_e32 v13, 0xffff0000, v118
	v_fmac_f32_e32 v11, v12, v12
	v_fmac_f32_e32 v11, v13, v13
	v_lshlrev_b32_e32 v12, 16, v119
	v_and_b32_e32 v13, 0xffff0000, v119
	v_fmac_f32_e32 v11, v12, v12
	v_fmac_f32_e32 v11, v13, v13
	ds_write_b32 v3, v11 offset:1360
	v_lshlrev_b32_e32 v8, 16, v120
	v_and_b32_e32 v9, 0xffff0000, v120
	v_mul_f32_e32 v7, v8, v8
	v_fmac_f32_e32 v7, v9, v9
	v_lshlrev_b32_e32 v8, 16, v121
	v_and_b32_e32 v9, 0xffff0000, v121
	v_fmac_f32_e32 v7, v8, v8
	v_fmac_f32_e32 v7, v9, v9
	v_lshlrev_b32_e32 v8, 16, v122
	v_and_b32_e32 v9, 0xffff0000, v122
	v_fmac_f32_e32 v7, v8, v8
	v_fmac_f32_e32 v7, v9, v9
	v_lshlrev_b32_e32 v8, 16, v123
	v_and_b32_e32 v9, 0xffff0000, v123
	v_fmac_f32_e32 v7, v8, v8
	v_fmac_f32_e32 v7, v9, v9
	ds_write_b32 v3, v7 offset:1632
	v_lshlrev_b32_e32 v12, 16, v124
	v_and_b32_e32 v13, 0xffff0000, v124
	v_mul_f32_e32 v11, v12, v12
	v_fmac_f32_e32 v11, v13, v13
	v_lshlrev_b32_e32 v12, 16, v125
	v_and_b32_e32 v13, 0xffff0000, v125
	v_fmac_f32_e32 v11, v12, v12
	v_fmac_f32_e32 v11, v13, v13
	v_lshlrev_b32_e32 v12, 16, v126
	v_and_b32_e32 v13, 0xffff0000, v126
	v_fmac_f32_e32 v11, v12, v12
	v_fmac_f32_e32 v11, v13, v13
	v_lshlrev_b32_e32 v12, 16, v127
	v_and_b32_e32 v13, 0xffff0000, v127
	v_fmac_f32_e32 v11, v12, v12
	v_fmac_f32_e32 v11, v13, v13
	ds_write_b32 v3, v11 offset:1904
	s_waitcnt vmcnt(16)
; __device__ __forceinline__ float bflo(unsigned w) { return __uint_as_float(w << 16); }
; __device__ __forceinline__ float bfhi(unsigned w) { return __uint_as_float(w & 0xffff0000u); }
; __global__ void __launch_bounds__(NTHR, 2) mega_fwd(Args args) {
;     ...
; #pragma unroll
;                       for (int i = 0; i < 16; ++i) { const u32x4 w = wq[i]; ss += (bflo(w.x) * bflo(w.x) + bfhi(w.x) * bfhi(w.x)) + (bflo(w.y) * bflo(w.y) + bfhi(w.y) * bfhi(w.y)) + (bflo(w.z) * bflo(w.z) + bfhi(w.z) * bfhi(w.z)) + (bflo(w.w) * bflo(w.w) + bfhi(w.w) * bfhi(w.w)); } }
	v_lshlrev_b32_e32 v8, 16, v128
	v_and_b32_e32 v9, 0xffff0000, v128
	v_mul_f32_e32 v7, v8, v8
	v_fmac_f32_e32 v7, v9, v9
	v_lshlrev_b32_e32 v8, 16, v129
	v_and_b32_e32 v9, 0xffff0000, v129
	v_fmac_f32_e32 v7, v8, v8
	v_fmac_f32_e32 v7, v9, v9
	v_lshlrev_b32_e32 v8, 16, v130
	v_and_b32_e32 v9, 0xffff0000, v130
	v_fmac_f32_e32 v7, v8, v8
	v_fmac_f32_e32 v7, v9, v9
	v_lshlrev_b32_e32 v8, 16, v131
	v_and_b32_e32 v9, 0xffff0000, v131
	v_fmac_f32_e32 v7, v8, v8
	v_fmac_f32_e32 v7, v9, v9
	ds_write_b32 v3, v7 offset:2176
	v_lshlrev_b32_e32 v12, 16, v132
	v_and_b32_e32 v13, 0xffff0000, v132
	v_mul_f32_e32 v11, v12, v12
	v_fmac_f32_e32 v11, v13, v13
	v_lshlrev_b32_e32 v12, 16, v133
	v_and_b32_e32 v13, 0xffff0000, v133
	v_fmac_f32_e32 v11, v12, v12
	v_fmac_f32_e32 v11, v13, v13
	v_lshlrev_b32_e32 v12, 16, v134
	v_and_b32_e32 v13, 0xffff0000, v134
	v_fmac_f32_e32 v11, v12, v12
	v_fmac_f32_e32 v11, v13, v13
	v_lshlrev_b32_e32 v12, 16, v135
	v_and_b32_e32 v13, 0xffff0000, v135
	v_fmac_f32_e32 v11, v12, v12
	v_fmac_f32_e32 v11, v13, v13
	ds_write_b32 v3, v11 offset:2448
	v_lshlrev_b32_e32 v8, 16, v136
	v_and_b32_e32 v9, 0xffff0000, v136
	v_mul_f32_e32 v7, v8, v8
	v_fmac_f32_e32 v7, v9, v9
	v_lshlrev_b32_e32 v8, 16, v137
	v_and_b32_e32 v9, 0xffff0000, v137
	v_fmac_f32_e32 v7, v8, v8
	v_fmac_f32_e32 v7, v9, v9
	v_lshlrev_b32_e32 v8, 16, v138
	v_and_b32_e32 v9, 0xffff0000, v138
	v_fmac_f32_e32 v7, v8, v8
	v_fmac_f32_e32 v7, v9, v9
	v_lshlrev_b32_e32 v8, 16, v139
	v_and_b32_e32 v9, 0xffff0000, v139
	v_fmac_f32_e32 v7, v8, v8
	v_fmac_f32_e32 v7, v9, v9
	ds_write_b32 v3, v7 offset:2720
	v_lshlrev_b32_e32 v12, 16, v140
	v_and_b32_e32 v13, 0xffff0000, v140
	v_mul_f32_e32 v11, v12, v12
	v_fmac_f32_e32 v11, v13, v13
	v_lshlrev_b32_e32 v12, 16, v141
	v_and_b32_e32 v13, 0xffff0000, v141
	v_fmac_f32_e32 v11, v12, v12
	v_fmac_f32_e32 v11, v13, v13
	v_lshlrev_b32_e32 v12, 16, v142
	v_and_b32_e32 v13, 0xffff0000, v142
	v_fmac_f32_e32 v11, v12, v12
	v_fmac_f32_e32 v11, v13, v13
	v_lshlrev_b32_e32 v12, 16, v143
	v_and_b32_e32 v13, 0xffff0000, v143
	v_fmac_f32_e32 v11, v12, v12
	v_fmac_f32_e32 v11, v13, v13
	ds_write_b32 v3, v11 offset:2992
	v_lshlrev_b32_e32 v8, 16, v144
	v_and_b32_e32 v9, 0xffff0000, v144
	v_mul_f32_e32 v7, v8, v8
	v_fmac_f32_e32 v7, v9, v9
	v_lshlrev_b32_e32 v8, 16, v145
	v_and_b32_e32 v9, 0xffff0000, v145
	v_fmac_f32_e32 v7, v8, v8
	v_fmac_f32_e32 v7, v9, v9
	v_lshlrev_b32_e32 v8, 16, v146
	v_and_b32_e32 v9, 0xffff0000, v146
	v_fmac_f32_e32 v7, v8, v8
	v_fmac_f32_e32 v7, v9, v9
	v_lshlrev_b32_e32 v8, 16, v147
	v_and_b32_e32 v9, 0xffff0000, v147
	v_fmac_f32_e32 v7, v8, v8
	v_fmac_f32_e32 v7, v9, v9
	ds_write_b32 v3, v7 offset:3264
	v_lshlrev_b32_e32 v12, 16, v148
	v_and_b32_e32 v13, 0xffff0000, v148
	v_mul_f32_e32 v11, v12, v12
	v_fmac_f32_e32 v11, v13, v13
	v_lshlrev_b32_e32 v12, 16, v149
	v_and_b32_e32 v13, 0xffff0000, v149
	v_fmac_f32_e32 v11, v12, v12
	v_fmac_f32_e32 v11, v13, v13
	v_lshlrev_b32_e32 v12, 16, v150
	v_and_b32_e32 v13, 0xffff0000, v150
	v_fmac_f32_e32 v11, v12, v12
	v_fmac_f32_e32 v11, v13, v13
	v_lshlrev_b32_e32 v12, 16, v151
	v_and_b32_e32 v13, 0xffff0000, v151
	v_fmac_f32_e32 v11, v12, v12
	v_fmac_f32_e32 v11, v13, v13
	ds_write_b32 v3, v11 offset:3536
	v_lshlrev_b32_e32 v8, 16, v152
	v_and_b32_e32 v9, 0xffff0000, v152
	v_mul_f32_e32 v7, v8, v8
	v_fmac_f32_e32 v7, v9, v9
	v_lshlrev_b32_e32 v8, 16, v153
	v_and_b32_e32 v9, 0xffff0000, v153
	v_fmac_f32_e32 v7, v8, v8
	v_fmac_f32_e32 v7, v9, v9
	v_lshlrev_b32_e32 v8, 16, v154
	v_and_b32_e32 v9, 0xffff0000, v154
	v_fmac_f32_e32 v7, v8, v8
	v_fmac_f32_e32 v7, v9, v9
	v_lshlrev_b32_e32 v8, 16, v155
	v_and_b32_e32 v9, 0xffff0000, v155
	v_fmac_f32_e32 v7, v8, v8
	v_fmac_f32_e32 v7, v9, v9
	ds_write_b32 v3, v7 offset:3808
	v_lshlrev_b32_e32 v12, 16, v156
	v_and_b32_e32 v13, 0xffff0000, v156
	v_mul_f32_e32 v11, v12, v12
	v_fmac_f32_e32 v11, v13, v13
	v_lshlrev_b32_e32 v12, 16, v157
	v_and_b32_e32 v13, 0xffff0000, v157
	v_fmac_f32_e32 v11, v12, v12
	v_fmac_f32_e32 v11, v13, v13
	v_lshlrev_b32_e32 v12, 16, v158
	v_and_b32_e32 v13, 0xffff0000, v158
	v_fmac_f32_e32 v11, v12, v12
	v_fmac_f32_e32 v11, v13, v13
	v_lshlrev_b32_e32 v12, 16, v159
	v_and_b32_e32 v13, 0xffff0000, v159
	v_fmac_f32_e32 v11, v12, v12
	v_fmac_f32_e32 v11, v13, v13
	ds_write_b32 v3, v11 offset:4080
	s_waitcnt vmcnt(8)
; __device__ __forceinline__ float bflo(unsigned w) { return __uint_as_float(w << 16); }
; __device__ __forceinline__ float bfhi(unsigned w) { return __uint_as_float(w & 0xffff0000u); }
; __global__ void __launch_bounds__(NTHR, 2) mega_fwd(Args args) {
;     ...
; #pragma unroll
;                       for (int i = 0; i < 16; ++i) { const u32x4 w = wq[i]; ss += (bflo(w.x) * bflo(w.x) + bfhi(w.x) * bfhi(w.x)) + (bflo(w.y) * bflo(w.y) + bfhi(w.y) * bfhi(w.y)) + (bflo(w.z) * bflo(w.z) + bfhi(w.z) * bfhi(w.z)) + (bflo(w.w) * bflo(w.w) + bfhi(w.w) * bfhi(w.w)); } }
	v_lshlrev_b32_e32 v8, 16, v160
	v_and_b32_e32 v9, 0xffff0000, v160
	v_mul_f32_e32 v7, v8, v8
	v_fmac_f32_e32 v7, v9, v9
	v_lshlrev_b32_e32 v8, 16, v161
	v_and_b32_e32 v9, 0xffff0000, v161
	v_fmac_f32_e32 v7, v8, v8
	v_fmac_f32_e32 v7, v9, v9
	v_lshlrev_b32_e32 v8, 16, v162
	v_and_b32_e32 v9, 0xffff0000, v162
	v_fmac_f32_e32 v7, v8, v8
	v_fmac_f32_e32 v7, v9, v9
	v_lshlrev_b32_e32 v8, 16, v163
	v_and_b32_e32 v9, 0xffff0000, v163
	v_fmac_f32_e32 v7, v8, v8
	v_fmac_f32_e32 v7, v9, v9
	ds_write_b32 v3, v7 offset:4352
	v_lshlrev_b32_e32 v12, 16, v164
	v_and_b32_e32 v13, 0xffff0000, v164
	v_mul_f32_e32 v11, v12, v12
	v_fmac_f32_e32 v11, v13, v13
	v_lshlrev_b32_e32 v12, 16, v165
	v_and_b32_e32 v13, 0xffff0000, v165
	v_fmac_f32_e32 v11, v12, v12
	v_fmac_f32_e32 v11, v13, v13
	v_lshlrev_b32_e32 v12, 16, v166
	v_and_b32_e32 v13, 0xffff0000, v166
	v_fmac_f32_e32 v11, v12, v12
	v_fmac_f32_e32 v11, v13, v13
	v_lshlrev_b32_e32 v12, 16, v167
	v_and_b32_e32 v13, 0xffff0000, v167
	v_fmac_f32_e32 v11, v12, v12
	v_fmac_f32_e32 v11, v13, v13
	ds_write_b32 v3, v11 offset:4624
	v_lshlrev_b32_e32 v8, 16, v168
	v_and_b32_e32 v9, 0xffff0000, v168
	v_mul_f32_e32 v7, v8, v8
	v_fmac_f32_e32 v7, v9, v9
	v_lshlrev_b32_e32 v8, 16, v169
	v_and_b32_e32 v9, 0xffff0000, v169
	v_fmac_f32_e32 v7, v8, v8
	v_fmac_f32_e32 v7, v9, v9
	v_lshlrev_b32_e32 v8, 16, v170
	v_and_b32_e32 v9, 0xffff0000, v170
	v_fmac_f32_e32 v7, v8, v8
	v_fmac_f32_e32 v7, v9, v9
	v_lshlrev_b32_e32 v8, 16, v171
	v_and_b32_e32 v9, 0xffff0000, v171
	v_fmac_f32_e32 v7, v8, v8
	v_fmac_f32_e32 v7, v9, v9
	ds_write_b32 v3, v7 offset:4896
	v_lshlrev_b32_e32 v12, 16, v172
	v_and_b32_e32 v13, 0xffff0000, v172
	v_mul_f32_e32 v11, v12, v12
	v_fmac_f32_e32 v11, v13, v13
	v_lshlrev_b32_e32 v12, 16, v173
	v_and_b32_e32 v13, 0xffff0000, v173
	v_fmac_f32_e32 v11, v12, v12
	v_fmac_f32_e32 v11, v13, v13
	v_lshlrev_b32_e32 v12, 16, v174
	v_and_b32_e32 v13, 0xffff0000, v174
	v_fmac_f32_e32 v11, v12, v12
	v_fmac_f32_e32 v11, v13, v13
	v_lshlrev_b32_e32 v12, 16, v175
	v_and_b32_e32 v13, 0xffff0000, v175
	v_fmac_f32_e32 v11, v12, v12
	v_fmac_f32_e32 v11, v13, v13
	ds_write_b32 v3, v11 offset:5168
	v_lshlrev_b32_e32 v8, 16, v176
	v_and_b32_e32 v9, 0xffff0000, v176
	v_mul_f32_e32 v7, v8, v8
	v_fmac_f32_e32 v7, v9, v9
	v_lshlrev_b32_e32 v8, 16, v177
	v_and_b32_e32 v9, 0xffff0000, v177
	v_fmac_f32_e32 v7, v8, v8
	v_fmac_f32_e32 v7, v9, v9
	v_lshlrev_b32_e32 v8, 16, v178
	v_and_b32_e32 v9, 0xffff0000, v178
	v_fmac_f32_e32 v7, v8, v8
	v_fmac_f32_e32 v7, v9, v9
	v_lshlrev_b32_e32 v8, 16, v179
	v_and_b32_e32 v9, 0xffff0000, v179
	v_fmac_f32_e32 v7, v8, v8
	v_fmac_f32_e32 v7, v9, v9
	ds_write_b32 v3, v7 offset:5440
	v_lshlrev_b32_e32 v12, 16, v180
	v_and_b32_e32 v13, 0xffff0000, v180
	v_mul_f32_e32 v11, v12, v12
	v_fmac_f32_e32 v11, v13, v13
	v_lshlrev_b32_e32 v12, 16, v181
	v_and_b32_e32 v13, 0xffff0000, v181
	v_fmac_f32_e32 v11, v12, v12
	v_fmac_f32_e32 v11, v13, v13
	v_lshlrev_b32_e32 v12, 16, v182
	v_and_b32_e32 v13, 0xffff0000, v182
	v_fmac_f32_e32 v11, v12, v12
	v_fmac_f32_e32 v11, v13, v13
	v_lshlrev_b32_e32 v12, 16, v183
	v_and_b32_e32 v13, 0xffff0000, v183
	v_fmac_f32_e32 v11, v12, v12
	v_fmac_f32_e32 v11, v13, v13
	ds_write_b32 v3, v11 offset:5712
	v_lshlrev_b32_e32 v8, 16, v184
	v_and_b32_e32 v9, 0xffff0000, v184
	v_mul_f32_e32 v7, v8, v8
	v_fmac_f32_e32 v7, v9, v9
	v_lshlrev_b32_e32 v8, 16, v185
	v_and_b32_e32 v9, 0xffff0000, v185
	v_fmac_f32_e32 v7, v8, v8
	v_fmac_f32_e32 v7, v9, v9
	v_lshlrev_b32_e32 v8, 16, v186
	v_and_b32_e32 v9, 0xffff0000, v186
	v_fmac_f32_e32 v7, v8, v8
	v_fmac_f32_e32 v7, v9, v9
	v_lshlrev_b32_e32 v8, 16, v187
	v_and_b32_e32 v9, 0xffff0000, v187
	v_fmac_f32_e32 v7, v8, v8
	v_fmac_f32_e32 v7, v9, v9
	ds_write_b32 v3, v7 offset:5984
	v_lshlrev_b32_e32 v12, 16, v188
	v_and_b32_e32 v13, 0xffff0000, v188
	v_mul_f32_e32 v11, v12, v12
	v_fmac_f32_e32 v11, v13, v13
	v_lshlrev_b32_e32 v12, 16, v189
	v_and_b32_e32 v13, 0xffff0000, v189
	v_fmac_f32_e32 v11, v12, v12
	v_fmac_f32_e32 v11, v13, v13
	v_lshlrev_b32_e32 v12, 16, v190
	v_and_b32_e32 v13, 0xffff0000, v190
	v_fmac_f32_e32 v11, v12, v12
	v_fmac_f32_e32 v11, v13, v13
	v_lshlrev_b32_e32 v12, 16, v191
	v_and_b32_e32 v13, 0xffff0000, v191
	v_fmac_f32_e32 v11, v12, v12
	v_fmac_f32_e32 v11, v13, v13
	ds_write_b32 v3, v11 offset:6256
	s_waitcnt vmcnt(0)
; #define LDS_WAIT() asm volatile("s_waitcnt lgkmcnt(0)" ::: "memory")
; __device__ __forceinline__ float bflo(unsigned w) { return __uint_as_float(w << 16); }
; __device__ __forceinline__ float bfhi(unsigned w) { return __uint_as_float(w & 0xffff0000u); }
; __global__ void __launch_bounds__(NTHR, 2) mega_fwd(Args args) {
;     ...
;                       for (int i = 0; i < 16; ++i) { const u32x4 w = wq[i]; ss += (bflo(w.x) * bflo(w.x) + bfhi(w.x) * bfhi(w.x)) + (bflo(w.y) * bflo(w.y) + bfhi(w.y) * bfhi(w.y)) + (bflo(w.z) * bflo(w.z) + bfhi(w.z) * bfhi(w.z)) + (bflo(w.w) * bflo(w.w) + bfhi(w.w) * bfhi(w.w)); } }
;                   ss = add_x<1>(ss); if (hf == 0) qrs[r] = 1.f / sqrtf(ss * (1.f / 512.f) + EPS); }
;               LDS_WAIT(); __syncthreads(); }
	v_lshlrev_b32_e32 v8, 16, v192
	v_and_b32_e32 v9, 0xffff0000, v192
	v_mul_f32_e32 v7, v8, v8
	v_fmac_f32_e32 v7, v9, v9
	v_lshlrev_b32_e32 v8, 16, v193
	v_and_b32_e32 v9, 0xffff0000, v193
	v_fmac_f32_e32 v7, v8, v8
	v_fmac_f32_e32 v7, v9, v9
	v_lshlrev_b32_e32 v8, 16, v194
	v_and_b32_e32 v9, 0xffff0000, v194
	v_fmac_f32_e32 v7, v8, v8
	v_fmac_f32_e32 v7, v9, v9
	v_lshlrev_b32_e32 v8, 16, v195
	v_and_b32_e32 v9, 0xffff0000, v195
	v_fmac_f32_e32 v7, v8, v8
	v_fmac_f32_e32 v7, v9, v9
	ds_write_b32 v3, v7 offset:6528
	v_lshlrev_b32_e32 v12, 16, v196
	v_and_b32_e32 v13, 0xffff0000, v196
	v_mul_f32_e32 v11, v12, v12
	v_fmac_f32_e32 v11, v13, v13
	v_lshlrev_b32_e32 v12, 16, v197
	v_and_b32_e32 v13, 0xffff0000, v197
	v_fmac_f32_e32 v11, v12, v12
	v_fmac_f32_e32 v11, v13, v13
	v_lshlrev_b32_e32 v12, 16, v198
	v_and_b32_e32 v13, 0xffff0000, v198
	v_fmac_f32_e32 v11, v12, v12
	v_fmac_f32_e32 v11, v13, v13
	v_lshlrev_b32_e32 v12, 16, v199
	v_and_b32_e32 v13, 0xffff0000, v199
	v_fmac_f32_e32 v11, v12, v12
	v_fmac_f32_e32 v11, v13, v13
	ds_write_b32 v3, v11 offset:6800
	v_lshlrev_b32_e32 v8, 16, v200
	v_and_b32_e32 v9, 0xffff0000, v200
	v_mul_f32_e32 v7, v8, v8
	v_fmac_f32_e32 v7, v9, v9
	v_lshlrev_b32_e32 v8, 16, v201
	v_and_b32_e32 v9, 0xffff0000, v201
	v_fmac_f32_e32 v7, v8, v8
	v_fmac_f32_e32 v7, v9, v9
	v_lshlrev_b32_e32 v8, 16, v202
	v_and_b32_e32 v9, 0xffff0000, v202
	v_fmac_f32_e32 v7, v8, v8
	v_fmac_f32_e32 v7, v9, v9
	v_lshlrev_b32_e32 v8, 16, v203
	v_and_b32_e32 v9, 0xffff0000, v203
	v_fmac_f32_e32 v7, v8, v8
	v_fmac_f32_e32 v7, v9, v9
	ds_write_b32 v3, v7 offset:7072
	v_lshlrev_b32_e32 v12, 16, v204
	v_and_b32_e32 v13, 0xffff0000, v204
	v_mul_f32_e32 v11, v12, v12
	v_fmac_f32_e32 v11, v13, v13
	v_lshlrev_b32_e32 v12, 16, v205
	v_and_b32_e32 v13, 0xffff0000, v205
	v_fmac_f32_e32 v11, v12, v12
	v_fmac_f32_e32 v11, v13, v13
	v_lshlrev_b32_e32 v12, 16, v206
	v_and_b32_e32 v13, 0xffff0000, v206
	v_fmac_f32_e32 v11, v12, v12
	v_fmac_f32_e32 v11, v13, v13
	v_lshlrev_b32_e32 v12, 16, v207
	v_and_b32_e32 v13, 0xffff0000, v207
	v_fmac_f32_e32 v11, v12, v12
	v_fmac_f32_e32 v11, v13, v13
	ds_write_b32 v3, v11 offset:7344
	v_lshlrev_b32_e32 v8, 16, v208
	v_and_b32_e32 v9, 0xffff0000, v208
	v_mul_f32_e32 v7, v8, v8
	v_fmac_f32_e32 v7, v9, v9
	v_lshlrev_b32_e32 v8, 16, v209
	v_and_b32_e32 v9, 0xffff0000, v209
	v_fmac_f32_e32 v7, v8, v8
	v_fmac_f32_e32 v7, v9, v9
	v_lshlrev_b32_e32 v8, 16, v210
	v_and_b32_e32 v9, 0xffff0000, v210
	v_fmac_f32_e32 v7, v8, v8
	v_fmac_f32_e32 v7, v9, v9
	v_lshlrev_b32_e32 v8, 16, v211
	v_and_b32_e32 v9, 0xffff0000, v211
	v_fmac_f32_e32 v7, v8, v8
	v_fmac_f32_e32 v7, v9, v9
	ds_write_b32 v3, v7 offset:7616
	v_lshlrev_b32_e32 v12, 16, v212
	v_and_b32_e32 v13, 0xffff0000, v212
	v_mul_f32_e32 v11, v12, v12
	v_fmac_f32_e32 v11, v13, v13
	v_lshlrev_b32_e32 v12, 16, v213
	v_and_b32_e32 v13, 0xffff0000, v213
	v_fmac_f32_e32 v11, v12, v12
	v_fmac_f32_e32 v11, v13, v13
	v_lshlrev_b32_e32 v12, 16, v214
	v_and_b32_e32 v13, 0xffff0000, v214
	v_fmac_f32_e32 v11, v12, v12
	v_fmac_f32_e32 v11, v13, v13
	v_lshlrev_b32_e32 v12, 16, v215
	v_and_b32_e32 v13, 0xffff0000, v215
	v_fmac_f32_e32 v11, v12, v12
	v_fmac_f32_e32 v11, v13, v13
	ds_write_b32 v3, v11 offset:7888
	v_lshlrev_b32_e32 v8, 16, v20
	v_and_b32_e32 v9, 0xffff0000, v20
	v_mul_f32_e32 v7, v8, v8
	v_fmac_f32_e32 v7, v9, v9
	v_lshlrev_b32_e32 v8, 16, v21
	v_and_b32_e32 v9, 0xffff0000, v21
	v_fmac_f32_e32 v7, v8, v8
	v_fmac_f32_e32 v7, v9, v9
	v_lshlrev_b32_e32 v8, 16, v22
	v_and_b32_e32 v9, 0xffff0000, v22
	v_fmac_f32_e32 v7, v8, v8
	v_fmac_f32_e32 v7, v9, v9
	v_lshlrev_b32_e32 v8, 16, v23
	v_and_b32_e32 v9, 0xffff0000, v23
	v_fmac_f32_e32 v7, v8, v8
	v_fmac_f32_e32 v7, v9, v9
	ds_write_b32 v3, v7 offset:8160
	v_lshlrev_b32_e32 v12, 16, v24
	v_and_b32_e32 v13, 0xffff0000, v24
	v_mul_f32_e32 v11, v12, v12
	v_fmac_f32_e32 v11, v13, v13
	v_lshlrev_b32_e32 v12, 16, v25
	v_and_b32_e32 v13, 0xffff0000, v25
	v_fmac_f32_e32 v11, v12, v12
	v_fmac_f32_e32 v11, v13, v13
	v_lshlrev_b32_e32 v12, 16, v26
	v_and_b32_e32 v13, 0xffff0000, v26
	v_fmac_f32_e32 v11, v12, v12
	v_fmac_f32_e32 v11, v13, v13
	v_lshlrev_b32_e32 v12, 16, v27
	v_and_b32_e32 v13, 0xffff0000, v27
	v_fmac_f32_e32 v11, v12, v12
	v_fmac_f32_e32 v11, v13, v13
	ds_write_b32 v3, v11 offset:8432
	s_waitcnt lgkmcnt(0)
	ds_read_b128 v[96:99], v5
	ds_read_b128 v[100:103], v5 offset:16
	ds_read_b128 v[104:107], v5 offset:32
	ds_read_b128 v[108:111], v5 offset:48
	ds_read_b128 v[112:115], v5 offset:64
	ds_read_b128 v[116:119], v5 offset:80
	ds_read_b128 v[120:123], v5 offset:96
	ds_read_b128 v[124:127], v5 offset:112
	s_waitcnt lgkmcnt(0)
	v_add_f32_e32 v7, v96, v97
	v_add_f32_e32 v7, v7, v98
	v_add_f32_e32 v7, v7, v99
	v_add_f32_e32 v7, v7, v100
	v_add_f32_e32 v7, v7, v101
	v_add_f32_e32 v7, v7, v102
	v_add_f32_e32 v7, v7, v103
	v_add_f32_e32 v7, v7, v104
	v_add_f32_e32 v7, v7, v105
	v_add_f32_e32 v7, v7, v106
	v_add_f32_e32 v7, v7, v107
	v_add_f32_e32 v7, v7, v108
	v_add_f32_e32 v7, v7, v109
	v_add_f32_e32 v7, v7, v110
	v_add_f32_e32 v7, v7, v111
	v_add_f32_e32 v7, v7, v112
	v_add_f32_e32 v7, v7, v113
	v_add_f32_e32 v7, v7, v114
	v_add_f32_e32 v7, v7, v115
	v_add_f32_e32 v7, v7, v116
	v_add_f32_e32 v7, v7, v117
	v_add_f32_e32 v7, v7, v118
	v_add_f32_e32 v7, v7, v119
	v_add_f32_e32 v7, v7, v120
	v_add_f32_e32 v7, v7, v121
	v_add_f32_e32 v7, v7, v122
	v_add_f32_e32 v7, v7, v123
	v_add_f32_e32 v7, v7, v124
	v_add_f32_e32 v7, v7, v125
	v_add_f32_e32 v7, v7, v126
	v_add_f32_e32 v7, v7, v127
	v_mov_b32_e32 v8, v7
	s_nop 1
	v_permlane32_swap_b32_e32 v7, v8
	s_nop 1
	v_add_f32_e32 v0, v7, v8
	v_fmamk_f32 v0, v0, 0x3b000000, v216
	v_mul_f32_e32 v2, 0x4f800000, v0
	v_cmp_gt_f32_e32 vcc, s28, v0
	s_nop 1
	v_cndmask_b32_e32 v0, v0, v2, vcc
	v_sqrt_f32_e32 v2, v0
	s_nop 0
	v_add_u32_e32 v3, -1, v2
	v_fma_f32 v5, -v3, v2, v0
	v_add_u32_e32 v4, 1, v2
	v_cmp_ge_f32_e64 s[58:59], 0, v5
	s_nop 1
	v_cndmask_b32_e64 v3, v2, v3, s[58:59]
	v_fma_f32 v2, -v4, v2, v0
	v_cmp_lt_f32_e64 s[58:59], 0, v2
	s_nop 1
	v_cndmask_b32_e64 v2, v3, v4, s[58:59]
	v_mul_f32_e32 v3, 0x37800000, v2
	v_cndmask_b32_e32 v2, v2, v3, vcc
	v_cmp_class_f32_e32 vcc, v0, v217
	s_nop 1
	v_cndmask_b32_e32 v0, v2, v0, vcc
	v_div_scale_f32 v2, s[8:9], v0, v0, 1.0
	v_rcp_f32_e32 v3, v2
	s_nop 0
	v_fma_f32 v4, -v2, v3, 1.0
	v_fmac_f32_e32 v3, v4, v3
	v_div_scale_f32 v4, vcc, 1.0, v0, 1.0
	v_mul_f32_e32 v5, v4, v3
	v_fma_f32 v6, -v2, v5, v4
	v_fmac_f32_e32 v5, v6, v3
	v_fma_f32 v2, -v2, v5, v4
	v_div_fmas_f32 v2, v2, v3, v5
	v_div_fixup_f32 v0, v2, v0, 1.0
	v_mbcnt_lo_u32_b32 v2, -1, 0
	v_mbcnt_hi_u32_b32 v2, -1, v2
	v_and_b32_e32 v2, 31, v2
	s_lshl_b32 s8, s87, 1
	v_lshl_add_u32 v2, v2, 2, s8
	v_add_u32_e32 v2, 0x20800, v2
	ds_write_b32 v2, v0
	s_mov_b64 s[36:37], 16
